# combined: queue prefetch + FoX prologue batching + max3 nop removal + setprio pair removal on best stack
# speedup vs baseline: 1.0053x; 1.0053x over previous
.LBB0_479:
	s_or_b64 exec, exec, s[2:3]
	s_mov_b32 s100, 1
	s_waitcnt lgkmcnt(0)
	s_barrier
	ds_read_b32 v1, v205
	s_mov_b64 s[2:3], -1
	s_waitcnt lgkmcnt(0)
	v_cmp_le_i32_e32 vcc, s29, v1
	v_readfirstlane_b32 s4, v1
	s_cbranch_vccnz .LBB0_474
	s_add_i32 s2, s4, 0xfffffe00
	s_cmpk_gt_i32 s4, 0x1ff
	s_cselect_b32 s2, s2, s4
	s_ashr_i32 s3, s2, 31
	s_lshr_b32 s3, s3, 26
	s_add_i32 s3, s2, s3
	s_ashr_i32 s52, s3, 6
	s_andn2_b32 s3, s3, 63
	s_sub_i32 s2, s2, s3
	v_mov_b32_e32 v1, v0
	s_ashr_i32 s20, s2, 2
	s_lshl_b32 s2, s2, 1
	v_readfirstlane_b32 s56, v1
	s_ashr_i32 s50, s56, 6
	s_ashr_i32 s51, s56, 8
	s_and_b32 s55, s2, 6
	s_sub_i32 s54, 7, s52
	s_and_b32 s53, s50, 3
	s_add_i32 s3, s51, s55
	s_ashr_i32 s21, s20, 31
	s_lshl_b32 s2, s54, 8
	s_lshl_b32 s57, s53, 6
	s_lshl_b32 s18, s3, 6
	s_or_b32 s6, s57, s2
	s_lshl_b64 s[4:5], s[20:21], 20
	s_ashr_i32 s19, s18, 31
	s_add_u32 s4, s4, s18
	v_and_b32_e32 v230, 31, v1
	s_addc_u32 s5, s5, s19
	v_or_b32_e32 v2, s6, v230
	s_lshl_b64 s[22:23], s[4:5], 1
	v_or_b32_e32 v4, 32, v2
	s_add_u32 s4, s30, s22
	v_mov_b32_e32 v5, v3
	s_addc_u32 s5, s31, s23
	v_lshlrev_b64 v[6:7], 10, v[2:3]
	v_lshlrev_b64 v[4:5], 10, v[4:5]
	s_lshl_b32 s58, s20, 3
	v_lshl_add_u64 v[6:7], s[4:5], 0, v[6:7]
	v_lshl_add_u64 v[4:5], s[4:5], 0, v[4:5]
	s_add_i32 s4, s3, s58
	s_ashr_i32 s5, s4, 31
	v_bfe_u32 v229, v1, 5, 1
	s_lshl_b64 s[4:5], s[4:5], 13
	v_lshlrev_b32_e32 v8, 4, v229
	v_mov_b32_e32 v9, v3
	s_add_u32 s4, s33, s4
	v_lshl_add_u64 v[4:5], v[4:5], 0, v[8:9]
	s_addc_u32 s5, s34, s5
	v_lshl_add_u64 v[6:7], v[6:7], 0, v[8:9]
	v_lshl_add_u64 v[8:9], v[2:3], 2, s[4:5]
	global_load_dwordx4 v[162:165], v[4:5], off offset:96
	global_load_dwordx4 v[166:169], v[4:5], off offset:64
	global_load_dwordx4 v[170:173], v[6:7], off offset:96
	global_load_dwordx4 v[174:177], v[6:7], off offset:64
	global_load_dwordx4 v[178:181], v[4:5], off offset:32
	global_load_dwordx4 v[182:185], v[4:5], off
	global_load_dwordx4 v[186:189], v[6:7], off offset:32
	global_load_dwordx4 v[190:193], v[6:7], off
	global_load_dword v232, v[8:9], off offset:128
	global_load_dword v233, v[8:9], off
	s_or_b32 s24, s55, s58
	s_ashr_i32 s25, s24, 31
	s_add_i32 s59, s58, 0x80
	s_lshl_b64 s[26:27], s[24:25], 13
	s_add_u32 s26, s33, s26
	s_addc_u32 s27, s34, s27
	s_lshl_b64 s[60:61], s[24:25], 2
	s_add_u32 s60, s35, s60
	s_mov_b32 s5, s7
	s_addc_u32 s61, s38, s61
	s_or_b32 s4, s59, s55
	v_mov_b32_e32 v2, v3
	v_mov_b32_e32 v4, v3
	s_lshl_b64 s[4:5], s[4:5], 2
	s_add_u32 s4, s35, s4
	s_addc_u32 s5, s38, s5
	s_mov_b32 s3, s7
	v_lshlrev_b32_e32 v5, 8, v230
	v_mov_b32_e32 v234, 0
	global_load_dword v2, v3, s[60:61]
	global_load_dword v4, v3, s[4:5]
	s_lshl_b64 s[4:5], s[2:3], 2
	s_add_u32 s2, s26, s4
	s_addc_u32 s3, s27, s5
	v_mov_b32_e32 v118, 0x2000
	v_add_u32_e32 v119, 0x2000, v5
	global_load_dword v6, v3, s[2:3]
	s_nop 0
	global_load_dword v5, v5, s[26:27] offset:252
	s_lshl_b64 s[98:99], s[6:7], 2
	s_add_u32 s98, s26, s98
	s_addc_u32 s99, s27, s99
	global_load_dword v114, v3, s[60:61] offset:4
	global_load_dword v115, v3, s[60:61] offset:516
	global_load_dword v116, v118, s[2:3]
	global_load_dword v117, v119, s[26:27] offset:252
	global_load_dword v120, v3, s[98:99]
	global_load_dword v121, v118, s[98:99]
	s_cmpk_gt_u32 s56, 0xff
	s_waitcnt vmcnt(2)
	v_mul_f32_e32 v2, v2, v4
	v_mul_f32_e32 v4, 0x4f800000, v2
	v_cmp_gt_f32_e32 vcc, s44, v2
	s_waitcnt vmcnt(0)
	v_sub_f32_e32 v5, v6, v5
	v_cndmask_b32_e32 v2, v2, v4, vcc
	v_sqrt_f32_e32 v4, v2
	s_nop 0
	v_add_u32_e32 v6, -1, v4
	v_add_u32_e32 v7, 1, v4
	v_fma_f32 v8, -v6, v4, v2
	v_fma_f32 v9, -v7, v4, v2
	v_cmp_ge_f32_e64 s[2:3], 0, v8
	s_nop 1
	v_cndmask_b32_e64 v4, v4, v6, s[2:3]
	v_cmp_lt_f32_e64 s[2:3], 0, v9
	s_nop 1
	v_cndmask_b32_e64 v4, v4, v7, s[2:3]
	v_mul_f32_e32 v6, 0x37800000, v4
	v_cndmask_b32_e32 v4, v4, v6, vcc
	v_cmp_class_f32_e32 vcc, v2, v226
	s_nop 1
	v_cndmask_b32_e32 v2, v4, v2, vcc
	v_fmac_f32_e32 v5, 2.0, v2
	v_cmp_le_f32_e32 vcc, s45, v5
	s_cbranch_scc1 .LBB0_482
	s_lshl_b64 s[2:3], s[6:7], 2
	s_add_u32 s2, s26, s2
	s_addc_u32 s3, s27, s3
	v_mov_b32_e32 v4, v120
	v_add_f32_e32 v2, v2, v2
	v_add_f32_e32 v2, 0x42480000, v2
	s_waitcnt vmcnt(0)
	v_add_f32_e32 v234, v2, v4

.LBB0_519:
	s_or_b64 exec, exec, s[2:3]
	s_mov_b32 s100, 2
	s_waitcnt lgkmcnt(0)
	s_barrier
	ds_read_b32 v2, v1
	s_mov_b64 s[2:3], -1
	s_waitcnt lgkmcnt(0)
	v_cmp_le_i32_e32 vcc, s29, v2
	v_readfirstlane_b32 s6, v2
	s_cbranch_vccnz .LBB0_514
	s_add_i32 s2, s6, 0xfffffe00
	s_cmpk_gt_i32 s6, 0x1ff
	s_cselect_b32 s2, s2, s6
	s_ashr_i32 s3, s2, 31
	s_lshr_b32 s3, s3, 26
	v_mov_b32_e32 v10, v0
	s_add_i32 s3, s2, s3
	s_ashr_i32 s42, s3, 6
	v_readfirstlane_b32 s34, v10
	s_andn2_b32 s3, s3, 63
	s_ashr_i32 s31, s34, 6
	s_sub_i32 s6, 7, s42
	s_sub_i32 s12, s2, s3
	s_and_b32 s13, s31, 3
	s_and_b32 s2, s12, 3
	s_ashr_i32 s14, s34, 8
	s_lshl_b32 s3, s6, 8
	s_lshl_b32 s43, s13, 6
	s_ashr_i32 s10, s12, 2
	s_or_b32 s30, s43, s3
	s_lshl_b32 s2, s2, 7
	s_lshl_b32 s3, s14, 6
	s_ashr_i32 s11, s10, 31
	s_add_i32 s2, s3, s2
	s_ashr_i32 s3, s2, 31
	s_lshl_b64 s[8:9], s[10:11], 21
	v_and_b32_e32 v203, 31, v10
	s_add_u32 s15, s18, s8
	v_or_b32_e32 v2, s30, v203
	s_addc_u32 s16, s19, s9
	s_lshl_b64 s[8:9], s[2:3], 1
	v_or_b32_e32 v4, 32, v2
	s_add_u32 s2, s15, s8
	v_mov_b32_e32 v5, v3
	v_bfe_u32 v202, v10, 5, 1
	s_addc_u32 s3, s16, s9
	v_lshlrev_b64 v[4:5], 10, v[4:5]
	v_lshlrev_b64 v[6:7], 10, v[2:3]
	v_lshlrev_b32_e32 v2, 4, v202
	v_lshl_add_u64 v[4:5], s[2:3], 0, v[4:5]
	v_lshl_add_u64 v[6:7], s[2:3], 0, v[6:7]
	v_lshl_add_u64 v[4:5], v[4:5], 0, v[2:3]
	v_lshl_add_u64 v[6:7], v[6:7], 0, v[2:3]
	global_load_dwordx4 v[162:165], v[4:5], off offset:96
	global_load_dwordx4 v[166:169], v[4:5], off offset:64
	global_load_dwordx4 v[170:173], v[6:7], off offset:96
	global_load_dwordx4 v[174:177], v[6:7], off offset:64
	global_load_dwordx4 v[178:181], v[4:5], off offset:32
	global_load_dwordx4 v[182:185], v[4:5], off
	global_load_dwordx4 v[186:189], v[6:7], off offset:32
	global_load_dwordx4 v[190:193], v[6:7], off
	s_lshl_b32 s40, s6, 2
	s_add_i32 s2, s40, -8
	s_cmp_gt_u32 s6, 2
	s_cselect_b32 s6, s2, 0
	s_lshl_b32 s12, s12, 6
	s_lshl_b64 s[2:3], s[10:11], 19
	s_and_b32 s12, s12, 0x80
	v_lshlrev_b32_e32 v6, 6, v10
	s_or_b32 s2, s2, s12
	v_and_b32_e32 v6, 0xf00, v6
	s_add_u32 s12, s20, s2
	v_and_b32_e32 v205, 63, v10
	v_lshl_or_b32 v6, s13, 12, v6
	s_addc_u32 s13, s21, s3
	v_mov_b32_e32 v5, v3
	v_lshlrev_b32_e32 v4, 8, v205
	s_add_u32 s2, s22, s2
	v_mov_b32_e32 v7, v3
	v_lshlrev_b32_e32 v204, 3, v10
	v_lshl_add_u64 v[4:5], s[12:13], 0, v[4:5]
	s_addc_u32 s3, s23, s3
	s_lshl_b32 s12, s31, 3
	s_lshl_b32 s14, s14, 5
	v_and_b32_e32 v15, 24, v204
	s_lshl_b32 s33, s31, 10
	s_ashr_i32 s13, s12, 31
	v_lshl_add_u64 v[6:7], s[2:3], 0, v[6:7]
	s_ashr_i32 s15, s14, 31
	v_mov_b32_e32 v9, v3
	v_lshlrev_b32_e32 v8, 1, v15
	s_lshl_b64 s[16:17], s[6:7], 14
	s_add_i32 s33, s33, 0
	v_lshl_add_u64 v[194:195], s[12:13], 1, v[4:5]
	v_lshl_add_u64 v[4:5], s[14:15], 1, v[6:7]
	v_mov_b32_e32 v11, v3
	v_mov_b32_e32 v12, v3
	v_mov_b32_e32 v13, v3
	v_mov_b32_e32 v14, v3
	s_add_i32 s2, s33, 0x8000
	v_lshl_add_u64 v[196:197], v[4:5], 0, v[8:9]
	v_lshl_add_u64 v[4:5], v[194:195], 0, s[16:17]
	s_mov_b32 m0, s33
	v_lshl_add_u64 v[6:7], v[196:197], 0, s[16:17]
	v_lshlrev_b32_e32 v206, 2, v202
	s_lshl_b32 s41, s6, 6
	v_mov_b32_e32 v16, v3
	v_mov_b32_e32 v17, v3
	v_mov_b32_e32 v8, v3
	v_mov_b32_e32 v211, 0
	s_add_i32 s35, s30, 0xfffffe00
	s_add_i32 s38, s30, 0xfffffe1f
	s_add_i32 s39, s30, 0xfffffe3f
	s_or_b32 s40, s40, 3
	s_barrier
	global_load_lds_dwordx4 v[4:5], off
	s_mov_b32 m0, s2
	s_and_b32 s2, s34, 0x3fffffc0
	global_load_lds_dwordx4 v[6:7], off
	s_lshl_b32 s2, s2, 2
	s_add_i32 s2, s2, 0
	s_add_i32 s12, s2, 0x10400
	v_lshlrev_b32_e32 v4, 1, v10
	v_lshrrev_b32_e32 v5, 2, v10
	v_lshl_add_u32 v200, v203, 2, s12
	v_add_u32_e32 v199, s12, v2
	s_lshl_b32 s12, s42, 8
	v_and_b32_e32 v4, 32, v4
	v_and_or_b32 v5, v5, 3, v206
	s_sub_i32 s12, s43, s12
	v_lshlrev_b32_e32 v5, 6, v5
	v_add_u32_e32 v2, 0, v4
	s_addk_i32 s12, 0x700
	v_add3_u32 v208, v2, v5, v15
	v_or_b32_e32 v2, s12, v203
	s_waitcnt vmcnt(0)
	v_lshlrev_b32_e32 v6, 10, v202
	v_lshlrev_b32_e32 v7, 4, v203
	v_sub_u32_e32 v2, v2, v206
	v_add3_u32 v207, 0, v6, v7
	v_subrev_u32_e32 v209, s41, v2
	v_mov_b32_e32 v2, v3
	v_mov_b32_e32 v4, v3
	v_mov_b32_e32 v5, v3
	v_mov_b32_e32 v6, v3
	v_mov_b32_e32 v7, v3
	v_mov_b32_e32 v10, v3
	v_mov_b32_e32 v11, v3
	v_mov_b32_e32 v12, v3
	v_mov_b32_e32 v13, v3
	v_mov_b32_e32 v14, v3
	v_mov_b32_e32 v15, v3
	v_mov_b64_e32 v[64:65], v[16:17]
	v_mov_b64_e32 v[80:81], v[16:17]
	v_mov_b64_e32 v[32:33], v[16:17]
	v_mov_b64_e32 v[48:49], v[16:17]
	s_or_b32 s34, s30, 63
	v_cmp_gt_u32_e64 s[2:3], 32, v205
	v_mov_b64_e32 v[62:63], v[14:15]
	v_mov_b64_e32 v[60:61], v[12:13]
	v_mov_b64_e32 v[58:59], v[10:11]
	v_mov_b64_e32 v[56:57], v[8:9]
	v_mov_b64_e32 v[54:55], v[6:7]
	v_mov_b64_e32 v[52:53], v[4:5]
	v_mov_b64_e32 v[50:51], v[2:3]
	v_mov_b64_e32 v[78:79], v[14:15]
	v_mov_b64_e32 v[76:77], v[12:13]
	v_mov_b64_e32 v[74:75], v[10:11]
	v_mov_b64_e32 v[72:73], v[8:9]
	v_mov_b64_e32 v[70:71], v[6:7]
	v_mov_b64_e32 v[68:69], v[4:5]
	v_mov_b64_e32 v[66:67], v[2:3]
	v_mov_b64_e32 v[30:31], v[14:15]
	v_mov_b64_e32 v[28:29], v[12:13]
	v_mov_b64_e32 v[26:27], v[10:11]
	v_mov_b64_e32 v[24:25], v[8:9]
	v_mov_b64_e32 v[22:23], v[6:7]
	v_mov_b64_e32 v[20:21], v[4:5]
	v_mov_b64_e32 v[18:19], v[2:3]
	v_mov_b64_e32 v[46:47], v[14:15]
	v_mov_b64_e32 v[44:45], v[12:13]
	v_mov_b64_e32 v[42:43], v[10:11]
	v_mov_b64_e32 v[40:41], v[8:9]
	v_mov_b64_e32 v[38:39], v[6:7]
	v_mov_b64_e32 v[36:37], v[4:5]
	v_mov_b64_e32 v[34:35], v[2:3]
	v_mov_b32_e32 v210, 0
	v_mov_b32_e32 v212, 0
	v_mov_b32_e32 v201, 0
	s_mov_b32 s12, s6
	v_mov_b32_e32 v82, 0
	v_mov_b32_e32 v83, v211
	v_mov_b32_e32 v84, v211
	v_mov_b32_e32 v85, v211
	v_mov_b32_e32 v86, v211
	v_mov_b32_e32 v87, v211
	v_mov_b32_e32 v88, v211
	v_mov_b32_e32 v89, v211
	v_mov_b32_e32 v90, v211
	v_mov_b32_e32 v91, v211
	v_mov_b32_e32 v92, v211
	v_mov_b32_e32 v93, v211
	v_mov_b32_e32 v94, v211
	v_mov_b32_e32 v95, v211
	v_mov_b32_e32 v96, v211
	v_mov_b32_e32 v97, v211
	s_waitcnt vmcnt(0) lgkmcnt(0)
	s_barrier
	s_branch .LBB0_524

.LBB0_553:
	s_or_b64 exec, exec, s[10:11]
	s_mov_b32 s100, 3
	v_mov_b32_e32 v2, s25
	s_waitcnt lgkmcnt(0)
	s_barrier
	ds_read_b32 v2, v2
	s_mov_b64 s[10:11], -1
	s_waitcnt lgkmcnt(0)
	v_readfirstlane_b32 s14, v2
	s_cmp_ge_i32 s14, s18
	s_cbranch_scc1 .LBB0_548
	s_add_i32 s10, s14, 0xfffffc00
	s_cmpk_gt_i32 s14, 0x3ff
	s_cselect_b32 s33, s10, s14
	s_ashr_i32 s10, s33, 6
	s_ashr_i32 s11, s10, 31
	s_bfe_u32 s14, s33, 0x10005
	v_readfirstlane_b32 s31, v0
	s_lshl_b64 s[16:17], s[10:11], 11
	s_lshl_b32 s10, s10, 1
	s_and_b32 s30, s33, 31
	s_lshr_b32 s39, s31, 6
	s_lshl_b32 s38, s14, 2
	s_or_b32 s14, s10, s14
	s_lshl_b32 s34, s30, 6
	s_lshl_b32 s35, s39, 3
	s_ashr_i32 s15, s14, 31
	s_add_i32 s29, s35, s34
	s_lshl_b64 s[10:11], s[14:15], 14
	s_add_u32 s40, s19, s10
	s_addc_u32 s41, s20, s11
	s_add_u32 s42, s21, s10
	s_addc_u32 s43, s22, s11
	s_lshl_b32 s10, s39, 4
	s_add_u32 s10, s40, s10
	s_addc_u32 s11, s41, 0
	s_lshr_b32 s31, s31, 2
	v_or_b32_e32 v76, s29, v67
	v_and_or_b32 v14, s31, 48, v71
	s_and_b32 s31, s31, 0x3fffffc0
	v_lshl_add_u64 v[2:3], s[16:17], 0, v[76:77]
	s_add_u32 s40, s42, s31
	v_or_b32_e32 v4, s38, v69
	v_lshlrev_b64 v[2:3], 10, v[2:3]
	s_addc_u32 s41, s43, 0
	v_mov_b32_e32 v89, v77
	v_mov_b32_e32 v91, v77
	v_lshl_add_u64 v[2:3], s[12:13], 0, v[2:3]
	v_lshlrev_b32_e32 v4, 7, v4
	v_mov_b32_e32 v5, v77
	v_lshl_add_u64 v[10:11], s[40:41], 0, v[88:89]
	v_lshl_add_u64 v[12:13], s[10:11], 0, v[90:91]
	v_lshlrev_b32_e32 v14, 7, v14
	v_mov_b32_e32 v15, v77
	v_lshl_add_u64 v[2:3], v[2:3], 0, v[4:5]
	v_mov_b32_e32 v87, v77
	v_lshl_add_u64 v[18:19], v[10:11], 0, v[14:15]
	v_add_co_u32_e32 v14, vcc, s26, v12
	v_lshl_add_u64 v[6:7], v[2:3], 0, v[86:87]
	s_nop 0
	v_addc_co_u32_e32 v15, vcc, 0, v13, vcc
	global_load_dwordx4 v[2:5], v[6:7], off
	global_load_dwordx4 v[92:95], v[6:7], off offset:32
	global_load_dwordx4 v[182:185], v[6:7], off offset:64
	global_load_dwordx4 v[186:189], v[6:7], off offset:96
	s_barrier
	global_load_dwordx4 v[6:9], v90, s[10:11]
	global_load_dwordx4 v[10:13], v[18:19], off
	s_nop 0
	global_load_dwordx4 v[14:17], v[14:15], off
	v_add_co_u32_e32 v18, vcc, s26, v18
	s_lshl_b32 s31, s39, 10
	s_nop 0
	v_addc_co_u32_e32 v19, vcc, 0, v19, vcc
	global_load_dwordx4 v[18:21], v[18:19], off
	v_add_u32_e32 v22, s31, v73
	v_subrev_co_u32_e64 v76, s[10:11], 31, v76
	v_lshrrev_b32_e32 v87, 4, v76
	v_add_u32_e32 v87, 1, v87
	v_cmp_gt_u32_e32 vcc, s27, v76
	v_mov_b32_e32 v203, v77
	s_waitcnt vmcnt(3)
	ds_write_b128 v22, v[6:9]
	s_waitcnt vmcnt(2)
	ds_write_b128 v22, v[10:13] offset:16384
	s_waitcnt vmcnt(1)
	ds_write_b128 v22, v[14:17] offset:8192
	s_waitcnt vmcnt(0)
	ds_write_b128 v22, v[18:21] offset:24576
	s_waitcnt lgkmcnt(0)
	s_barrier
	ds_read_b128 v[6:9], v177
	ds_read_b128 v[10:13], v177 offset:512
	s_waitcnt lgkmcnt(1)
	v_mfma_f32_32x32x16_bf16 v[50:65], v[6:9], v[2:5], 0
	v_cndmask_b32_e32 v76, v180, v87, vcc
	v_cndmask_b32_e64 v76, v76, 0, s[10:11]
	v_cmp_lt_u32_e32 vcc, v75, v76
	s_waitcnt lgkmcnt(0)
	v_mfma_f32_32x32x16_bf16 v[34:49], v[10:13], v[2:5], 0
	ds_read_b128 v[6:9], v177 offset:8192
	ds_read_b128 v[10:13], v177 offset:8704
	ds_read_b128 v[190:193], v177 offset:2048
	ds_read_b128 v[194:197], v177 offset:2560
	s_waitcnt lgkmcnt(3)
	v_mfma_f32_32x32x16_bf16 v[18:33], v[6:9], v[2:5], 0
	s_waitcnt lgkmcnt(2)
	v_mfma_f32_32x32x16_bf16 v[2:17], v[10:13], v[2:5], 0
	s_waitcnt lgkmcnt(1)
	v_mfma_f32_32x32x16_bf16 v[50:65], v[190:193], v[92:95], v[50:65]
	s_waitcnt lgkmcnt(0)
	v_mfma_f32_32x32x16_bf16 v[34:49], v[194:197], v[92:95], v[34:49]
	ds_read_b128 v[190:193], v177 offset:10240
	ds_read_b128 v[194:197], v177 offset:10752
	s_waitcnt lgkmcnt(1)
	v_mfma_f32_32x32x16_bf16 v[18:33], v[190:193], v[92:95], v[18:33]
	s_waitcnt lgkmcnt(0)
	v_mfma_f32_32x32x16_bf16 v[2:17], v[194:197], v[92:95], v[2:17]
	ds_read_b128 v[92:95], v177 offset:4096
	ds_read_b128 v[190:193], v177 offset:4608
	s_waitcnt lgkmcnt(1)
	v_mfma_f32_32x32x16_bf16 v[50:65], v[92:95], v[182:185], v[50:65]
	s_waitcnt lgkmcnt(0)
	v_mfma_f32_32x32x16_bf16 v[34:49], v[190:193], v[182:185], v[34:49]
	ds_read_b128 v[92:95], v177 offset:12288
	ds_read_b128 v[190:193], v177 offset:12800
	s_waitcnt lgkmcnt(1)
	v_mfma_f32_32x32x16_bf16 v[18:33], v[92:95], v[182:185], v[18:33]
	s_waitcnt lgkmcnt(0)
	v_mfma_f32_32x32x16_bf16 v[2:17], v[190:193], v[182:185], v[2:17]
	ds_read_b128 v[92:95], v177 offset:6144
	ds_read_b128 v[182:185], v177 offset:6656
	s_waitcnt lgkmcnt(1)
	v_mfma_f32_32x32x16_bf16 v[50:65], v[92:95], v[186:189], v[50:65]
	s_waitcnt lgkmcnt(0)
	v_mfma_f32_32x32x16_bf16 v[34:49], v[182:185], v[186:189], v[34:49]
	s_nop 9
	v_cndmask_b32_e32 v50, v178, v50, vcc
	v_cmp_lt_u32_e32 vcc, v81, v76
	ds_read_b128 v[92:95], v177 offset:14336
	ds_read_b128 v[182:185], v177 offset:14848
	v_cndmask_b32_e32 v51, v178, v51, vcc
	v_cmp_lt_u32_e32 vcc, v83, v76
	s_nop 1
	v_cndmask_b32_e32 v52, v178, v52, vcc
	v_cmp_lt_u32_e32 vcc, v85, v76
	s_waitcnt lgkmcnt(1)
	v_mfma_f32_32x32x16_bf16 v[18:33], v[92:95], v[186:189], v[18:33]
	v_cndmask_b32_e32 v53, v178, v53, vcc
	v_cmp_lt_u32_e32 vcc, v98, v76
	s_nop 1
	v_cndmask_b32_e32 v54, v178, v54, vcc
	v_cmp_lt_u32_e32 vcc, v99, v76
	s_waitcnt lgkmcnt(0)
	v_mfma_f32_32x32x16_bf16 v[2:17], v[182:185], v[186:189], v[2:17]
	v_cndmask_b32_e32 v55, v178, v55, vcc
	v_cmp_lt_u32_e32 vcc, v100, v76
	s_nop 1
	v_cndmask_b32_e32 v56, v178, v56, vcc
	v_cmp_lt_u32_e32 vcc, v101, v76
	s_nop 1
	v_cndmask_b32_e32 v57, v178, v57, vcc
	v_cmp_lt_u32_e32 vcc, v102, v76
	s_nop 1
	v_cndmask_b32_e32 v58, v178, v58, vcc
	v_cmp_lt_u32_e32 vcc, v103, v76
	s_nop 1
	v_cndmask_b32_e32 v59, v178, v59, vcc
	v_cmp_lt_u32_e32 vcc, v104, v76
	s_nop 1
	v_cndmask_b32_e32 v60, v178, v60, vcc
	v_cmp_lt_u32_e32 vcc, v105, v76
	s_nop 1
	v_cndmask_b32_e32 v61, v178, v61, vcc
	v_cmp_lt_u32_e32 vcc, v106, v76
	s_nop 1
	v_cndmask_b32_e32 v62, v178, v62, vcc
	v_cmp_lt_u32_e32 vcc, v107, v76
	s_nop 1
	v_cndmask_b32_e32 v63, v178, v63, vcc
	v_cmp_lt_u32_e32 vcc, v108, v76
	s_nop 1
	v_cndmask_b32_e32 v64, v178, v64, vcc
	v_cmp_lt_u32_e32 vcc, v109, v76
	s_nop 1
	v_cndmask_b32_e32 v65, v178, v65, vcc
	v_cmp_lt_u32_e32 vcc, v110, v76
	s_nop 1
	v_cndmask_b32_e32 v34, v178, v34, vcc
	v_cmp_lt_u32_e32 vcc, v111, v76
	s_nop 1
	v_cndmask_b32_e32 v35, v178, v35, vcc
	v_cmp_lt_u32_e32 vcc, v112, v76
	s_nop 1
	v_cndmask_b32_e32 v36, v178, v36, vcc
	v_cmp_lt_u32_e32 vcc, v113, v76
	s_nop 1
	v_cndmask_b32_e32 v37, v178, v37, vcc
	v_cmp_lt_u32_e32 vcc, v114, v76
	s_nop 1
	v_cndmask_b32_e32 v38, v178, v38, vcc
	v_cmp_lt_u32_e32 vcc, v115, v76
	s_nop 1
	v_cndmask_b32_e32 v39, v178, v39, vcc
	v_cmp_lt_u32_e32 vcc, v116, v76
	s_nop 1
	v_cndmask_b32_e32 v40, v178, v40, vcc
	v_cmp_lt_u32_e32 vcc, v117, v76
	s_nop 1
	v_cndmask_b32_e32 v41, v178, v41, vcc
	v_cmp_lt_u32_e32 vcc, v118, v76
	s_nop 1
	v_cndmask_b32_e32 v42, v178, v42, vcc
	v_cmp_lt_u32_e32 vcc, v119, v76
	s_nop 1
	v_cndmask_b32_e32 v43, v178, v43, vcc
	v_cmp_lt_u32_e32 vcc, v120, v76
	s_nop 1
	v_cndmask_b32_e32 v44, v178, v44, vcc
	v_cmp_lt_u32_e32 vcc, v121, v76
	s_nop 1
	v_cndmask_b32_e32 v45, v178, v45, vcc
	v_cmp_lt_u32_e32 vcc, v122, v76
	s_nop 1
	v_cndmask_b32_e32 v46, v178, v46, vcc
	v_cmp_lt_u32_e32 vcc, v123, v76
	s_nop 1
	v_cndmask_b32_e32 v47, v178, v47, vcc
	v_cmp_lt_u32_e32 vcc, v124, v76
	s_nop 1
	v_cndmask_b32_e32 v48, v178, v48, vcc
	v_cmp_lt_u32_e32 vcc, v125, v76
	s_nop 1
	v_cndmask_b32_e32 v49, v178, v49, vcc
	v_cmp_lt_u32_e32 vcc, v126, v76
	s_nop 1
	v_cndmask_b32_e32 v87, v178, v18, vcc
	v_cmp_lt_u32_e32 vcc, v127, v76
	s_nop 1
	v_cndmask_b32_e32 v89, v178, v19, vcc
	v_cmp_lt_u32_e32 vcc, v128, v76
	s_nop 1
	v_cndmask_b32_e32 v91, v178, v20, vcc
	v_cmp_lt_u32_e32 vcc, v129, v76
	s_nop 1
	v_cndmask_b32_e32 v92, v178, v21, vcc
	v_cmp_lt_u32_e32 vcc, v130, v76
	s_nop 1
	v_cndmask_b32_e32 v93, v178, v22, vcc
	v_cmp_lt_u32_e32 vcc, v131, v76
	s_nop 1
	v_cndmask_b32_e32 v94, v178, v23, vcc
	v_cmp_lt_u32_e32 vcc, v132, v76
	s_nop 1
	v_cndmask_b32_e32 v24, v178, v24, vcc
	v_cmp_lt_u32_e32 vcc, v133, v76
	s_nop 1
	v_cndmask_b32_e32 v25, v178, v25, vcc
	v_cmp_lt_u32_e32 vcc, v134, v76
	s_nop 1
	v_cndmask_b32_e32 v26, v178, v26, vcc
	v_cmp_lt_u32_e32 vcc, v135, v76
	s_nop 1
	v_cndmask_b32_e32 v27, v178, v27, vcc
	v_cmp_lt_u32_e32 vcc, v136, v76
	s_nop 1
	v_cndmask_b32_e32 v95, v178, v28, vcc
	v_cmp_lt_u32_e32 vcc, v137, v76
	s_nop 1
	v_cndmask_b32_e32 v96, v178, v29, vcc
	v_cmp_lt_u32_e32 vcc, v138, v76
	s_nop 1
	v_cndmask_b32_e32 v97, v178, v30, vcc
	v_cmp_lt_u32_e32 vcc, v139, v76
	s_nop 1
	v_cndmask_b32_e32 v183, v178, v31, vcc
	v_cmp_lt_u32_e32 vcc, v140, v76
	s_nop 1
	v_cndmask_b32_e32 v32, v178, v32, vcc
	v_cmp_lt_u32_e32 vcc, v141, v76
	s_nop 1
	v_cndmask_b32_e32 v33, v178, v33, vcc
	v_cmp_lt_u32_e32 vcc, v142, v76
	s_nop 1
	v_cndmask_b32_e32 v186, v178, v2, vcc
	v_cmp_lt_u32_e32 vcc, v143, v76
	v_max3_f32 v2, v178, v50, v51
	v_max3_f32 v2, v2, v54, v55
	s_nop 0
	v_cndmask_b32_e32 v187, v178, v3, vcc
	v_max3_f32 v3, v178, v52, v53
	v_cmp_lt_u32_e32 vcc, v144, v76
	v_max3_f32 v3, v3, v56, v57
	v_max3_f32 v2, v2, v58, v59
	v_max3_f32 v3, v3, v60, v61
	v_max3_f32 v2, v2, v62, v63
	s_nop 0
	v_cndmask_b32_e32 v188, v178, v4, vcc
	v_cmp_lt_u32_e32 vcc, v145, v76
	v_max3_f32 v3, v3, v64, v65
	v_max3_f32 v2, v2, v34, v35
	v_max3_f32 v3, v3, v36, v37
	v_max3_f32 v2, v2, v38, v39
	s_nop 0
	v_cndmask_b32_e32 v189, v178, v5, vcc
	v_cmp_lt_u32_e32 vcc, v146, v76
	v_max3_f32 v3, v3, v40, v41
	v_max3_f32 v2, v2, v42, v43
	v_max3_f32 v3, v3, v44, v45
	v_max3_f32 v2, v2, v46, v47
	s_nop 0
	v_cndmask_b32_e32 v190, v178, v6, vcc
	v_cmp_lt_u32_e32 vcc, v147, v76
	v_max3_f32 v3, v3, v48, v49
	v_max3_f32 v2, v2, v87, v89
	v_max3_f32 v3, v3, v91, v92
	v_max3_f32 v2, v2, v93, v94
	s_nop 0
	v_cndmask_b32_e32 v191, v178, v7, vcc
	v_cmp_lt_u32_e32 vcc, v148, v76
	v_max3_f32 v3, v3, v24, v25
	v_max3_f32 v2, v2, v26, v27
	v_max3_f32 v3, v3, v95, v96
	v_max3_f32 v2, v2, v97, v183
	s_nop 0
	v_cndmask_b32_e32 v8, v178, v8, vcc
	v_cmp_lt_u32_e32 vcc, v149, v76
	v_max3_f32 v3, v3, v32, v33
	v_max3_f32 v2, v2, v186, v187
	v_max3_f32 v3, v3, v188, v189
	v_max3_f32 v2, v2, v190, v191
	s_nop 0
	v_cndmask_b32_e32 v9, v178, v9, vcc
	v_cmp_lt_u32_e32 vcc, v150, v76
	v_max3_f32 v3, v3, v8, v9
	s_nop 1
	v_cndmask_b32_e32 v10, v178, v10, vcc
	v_cmp_lt_u32_e32 vcc, v151, v76
	s_nop 1
	v_cndmask_b32_e32 v11, v178, v11, vcc
	v_cmp_lt_u32_e32 vcc, v152, v76
	v_max3_f32 v2, v2, v10, v11
	s_nop 1
	v_cndmask_b32_e32 v196, v178, v12, vcc
	v_cmp_lt_u32_e32 vcc, v153, v76
	s_nop 1
	v_cndmask_b32_e32 v197, v178, v13, vcc
	v_cmp_lt_u32_e32 vcc, v154, v76
	v_max3_f32 v3, v3, v196, v197
	s_nop 1
	v_cndmask_b32_e32 v198, v178, v14, vcc
	v_cmp_lt_u32_e32 vcc, v155, v76
	s_nop 1
	v_cndmask_b32_e32 v199, v178, v15, vcc
	v_cmp_lt_u32_e32 vcc, v156, v76
	v_max3_f32 v2, v2, v198, v199
	s_nop 1
	v_cndmask_b32_e32 v200, v178, v16, vcc
	v_cmp_lt_u32_e32 vcc, v157, v76
	s_nop 1
	v_cndmask_b32_e32 v76, v178, v17, vcc
	v_max3_f32 v3, v3, v200, v76
	v_max3_f32 v2, v2, v3, v3
	v_mov_b32_e32 v3, v2
	s_nop 1
	v_permlane32_swap_b32_e32 v2, v3
	v_max_f32_e32 v3, v3, v3
	v_max_f32_e32 v2, v2, v2
	v_max_f32_e32 v2, v2, v3
	v_cndmask_b32_e64 v201, v2, 0, s[10:11]
	v_sub_f32_e32 v2, v50, v201
	v_exp_f32_e32 v2, v2
	v_sub_f32_e32 v3, v51, v201
	v_exp_f32_e32 v3, v3
	v_sub_f32_e32 v4, v52, v201
	v_exp_f32_e32 v4, v4
	v_sub_f32_e32 v5, v53, v201
	v_exp_f32_e32 v5, v5
	v_add_f32_e32 v6, 0, v2
	v_add_f32_e32 v6, v3, v6
	v_add_f32_e32 v6, v4, v6
	v_add_f32_e32 v14, v5, v6
	v_sub_f32_e32 v6, v54, v201
	v_exp_f32_e32 v6, v6
	v_sub_f32_e32 v7, v55, v201
	v_exp_f32_e32 v7, v7
	v_sub_f32_e32 v12, v56, v201
	v_exp_f32_e32 v12, v12
	v_sub_f32_e32 v13, v57, v201
	v_exp_f32_e32 v13, v13
	v_add_f32_e32 v14, v6, v14
	v_add_f32_e32 v14, v7, v14
	v_add_f32_e32 v14, v12, v14
	v_add_f32_e32 v18, v13, v14
	v_sub_f32_e32 v14, v58, v201
	v_exp_f32_e32 v14, v14
	v_sub_f32_e32 v15, v59, v201
	v_exp_f32_e32 v15, v15
	v_sub_f32_e32 v16, v60, v201
	v_exp_f32_e32 v16, v16
	v_sub_f32_e32 v17, v61, v201
	v_exp_f32_e32 v17, v17
	v_add_f32_e32 v18, v14, v18
	v_add_f32_e32 v18, v15, v18
	v_add_f32_e32 v18, v16, v18
	v_add_f32_e32 v22, v17, v18
	v_sub_f32_e32 v18, v62, v201
	v_exp_f32_e32 v18, v18
	v_sub_f32_e32 v19, v63, v201
	v_exp_f32_e32 v19, v19
	v_sub_f32_e32 v20, v64, v201
	v_exp_f32_e32 v20, v20
	v_sub_f32_e32 v21, v65, v201
	v_exp_f32_e32 v21, v21
	v_add_f32_e32 v22, v18, v22
	v_add_f32_e32 v22, v19, v22
	v_add_f32_e32 v22, v20, v22
	v_add_f32_e32 v30, v21, v22
	v_sub_f32_e32 v22, v34, v201
	v_exp_f32_e32 v22, v22
	v_sub_f32_e32 v23, v35, v201
	v_exp_f32_e32 v23, v23
	v_sub_f32_e32 v28, v36, v201
	v_exp_f32_e32 v28, v28
	v_sub_f32_e32 v29, v37, v201
	v_exp_f32_e32 v29, v29
	v_add_f32_e32 v30, v22, v30
	v_add_f32_e32 v30, v23, v30
	v_add_f32_e32 v30, v28, v30
	v_add_f32_e32 v36, v29, v30
	v_sub_f32_e32 v30, v38, v201
	v_exp_f32_e32 v30, v30
	v_sub_f32_e32 v31, v39, v201
	v_exp_f32_e32 v31, v31
	v_sub_f32_e32 v34, v40, v201
	v_exp_f32_e32 v34, v34
	v_sub_f32_e32 v35, v41, v201
	v_exp_f32_e32 v35, v35
	v_add_f32_e32 v36, v30, v36
	v_add_f32_e32 v36, v31, v36
	v_add_f32_e32 v36, v34, v36
	v_add_f32_e32 v40, v35, v36
	v_sub_f32_e32 v36, v42, v201
	v_exp_f32_e32 v36, v36
	v_sub_f32_e32 v37, v43, v201
	v_exp_f32_e32 v37, v37
	v_sub_f32_e32 v38, v44, v201
	v_exp_f32_e32 v38, v38
	v_sub_f32_e32 v39, v45, v201
	v_exp_f32_e32 v39, v39
	v_add_f32_e32 v40, v36, v40
	v_add_f32_e32 v40, v37, v40
	v_add_f32_e32 v40, v38, v40
	v_add_f32_e32 v44, v39, v40
	v_sub_f32_e32 v40, v46, v201
	v_exp_f32_e32 v40, v40
	v_sub_f32_e32 v41, v47, v201
	v_exp_f32_e32 v41, v41
	v_sub_f32_e32 v42, v48, v201
	v_exp_f32_e32 v42, v42
	v_sub_f32_e32 v43, v49, v201
	v_exp_f32_e32 v43, v43
	v_add_f32_e32 v44, v40, v44
	v_add_f32_e32 v44, v41, v44
	v_add_f32_e32 v44, v42, v44
	v_add_f32_e32 v48, v43, v44
	v_sub_f32_e32 v44, v87, v201
	v_exp_f32_e32 v44, v44
	v_sub_f32_e32 v45, v89, v201
	v_exp_f32_e32 v45, v45
	v_sub_f32_e32 v46, v91, v201
	v_exp_f32_e32 v46, v46
	v_sub_f32_e32 v47, v92, v201
	v_exp_f32_e32 v47, v47
	v_add_f32_e32 v48, v44, v48
	v_add_f32_e32 v48, v45, v48
	v_add_f32_e32 v48, v46, v48
	v_add_f32_e32 v52, v47, v48
	v_sub_f32_e32 v48, v93, v201
	v_exp_f32_e32 v48, v48
	v_sub_f32_e32 v49, v94, v201
	v_exp_f32_e32 v49, v49
	v_sub_f32_e32 v24, v24, v201
	v_exp_f32_e32 v50, v24
	v_sub_f32_e32 v24, v25, v201
	v_exp_f32_e32 v51, v24
	v_sub_f32_e32 v25, v26, v201
	v_add_f32_e32 v24, v48, v52
	v_exp_f32_e32 v52, v25
	v_sub_f32_e32 v25, v27, v201
	v_add_f32_e32 v24, v49, v24
	v_exp_f32_e32 v53, v25
	v_sub_f32_e32 v25, v95, v201
	v_add_f32_e32 v24, v50, v24
	v_exp_f32_e32 v54, v25
	v_sub_f32_e32 v25, v96, v201
	v_add_f32_e32 v24, v51, v24
	v_exp_f32_e32 v55, v25
	v_sub_f32_e32 v25, v97, v201
	v_add_f32_e32 v24, v52, v24
	v_exp_f32_e32 v182, v25
	v_sub_f32_e32 v25, v183, v201
	v_add_f32_e32 v24, v53, v24
	v_exp_f32_e32 v183, v25
	v_sub_f32_e32 v25, v32, v201
	v_add_f32_e32 v24, v54, v24
	v_exp_f32_e32 v184, v25
	v_sub_f32_e32 v25, v33, v201
	v_add_f32_e32 v24, v55, v24
	v_exp_f32_e32 v185, v25
	v_sub_f32_e32 v25, v186, v201
	v_add_f32_e32 v24, v182, v24
	v_exp_f32_e32 v186, v25
	v_sub_f32_e32 v25, v187, v201
	v_add_f32_e32 v24, v183, v24
	v_exp_f32_e32 v187, v25
	v_sub_f32_e32 v25, v188, v201
	v_add_f32_e32 v24, v184, v24
	v_exp_f32_e32 v188, v25
	v_sub_f32_e32 v25, v189, v201
	v_add_f32_e32 v24, v185, v24
	v_exp_f32_e32 v189, v25
	v_sub_f32_e32 v25, v190, v201
	v_add_f32_e32 v24, v186, v24
	v_exp_f32_e32 v190, v25
	v_sub_f32_e32 v25, v191, v201
	v_add_f32_e32 v24, v187, v24
	v_exp_f32_e32 v191, v25
	v_sub_f32_e32 v8, v8, v201
	v_add_f32_e32 v24, v188, v24
	v_exp_f32_e32 v192, v8
	v_sub_f32_e32 v8, v9, v201
	v_add_f32_e32 v24, v189, v24
	v_exp_f32_e32 v193, v8
	v_sub_f32_e32 v9, v10, v201
	v_add_f32_e32 v8, v190, v24
	v_exp_f32_e32 v194, v9
	v_sub_f32_e32 v9, v11, v201
	v_add_f32_e32 v8, v191, v8
	v_exp_f32_e32 v195, v9
	v_sub_f32_e32 v9, v196, v201
	v_add_f32_e32 v8, v192, v8
	v_exp_f32_e32 v196, v9
	v_sub_f32_e32 v9, v197, v201
	v_add_f32_e32 v8, v193, v8
	v_exp_f32_e32 v197, v9
	v_sub_f32_e32 v9, v198, v201
	v_add_f32_e32 v8, v194, v8
	v_exp_f32_e32 v198, v9
	v_sub_f32_e32 v9, v199, v201
	v_add_f32_e32 v8, v195, v8
	v_exp_f32_e32 v199, v9
	v_sub_f32_e32 v9, v200, v201
	v_add_f32_e32 v8, v196, v8
	v_exp_f32_e32 v200, v9
	v_sub_f32_e32 v9, v76, v201
	v_add_f32_e32 v8, v197, v8
	v_exp_f32_e32 v201, v9
	v_add_f32_e32 v8, v198, v8
	v_add_f32_e32 v8, v199, v8
	v_add_f32_e32 v8, v200, v8
	v_add_f32_e32 v8, v201, v8
	v_mov_b32_e32 v9, v8
	s_nop 1
	v_permlane32_swap_b32_e32 v8, v9
	v_add_f32_e32 v8, v8, v9
	v_div_scale_f32 v9, s[40:41], v8, v8, 1.0
	v_rcp_f32_e32 v10, v9
	s_add_i32 s40, s31, 0
	s_add_i32 s40, s40, 0x10a00
	v_fma_f32 v11, -v9, v10, 1.0
	v_fmac_f32_e32 v10, v11, v10
	v_div_scale_f32 v11, vcc, 1.0, v8, 1.0
	v_mul_f32_e32 v24, v11, v10
	v_fma_f32 v25, -v9, v24, v11
	v_fmac_f32_e32 v24, v25, v10
	v_fma_f32 v9, -v9, v24, v11
	v_div_fmas_f32 v9, v9, v10, v24
	v_div_fixup_f32 v8, v9, v8, 1.0
	v_cndmask_b32_e64 v76, v8, 0, s[10:11]
	v_pk_mul_f32 v[10:11], v[76:77], v[2:3] op_sel_hi:[0,1]
	v_pk_mul_f32 v[8:9], v[76:77], v[4:5] op_sel_hi:[0,1]
	v_pk_mul_f32 v[6:7], v[76:77], v[6:7] op_sel_hi:[0,1]
	v_pk_mul_f32 v[4:5], v[76:77], v[12:13] op_sel_hi:[0,1]
	v_add_f32_e32 v12, v8, v9
	v_add_f32_e32 v13, v10, v11
	v_pk_mul_f32 v[2:3], v[76:77], v[14:15] op_sel_hi:[0,1]
	v_pk_mul_f32 v[24:25], v[76:77], v[16:17] op_sel_hi:[0,1]
	v_add_f32_e32 v12, v13, v12
	v_add_f32_e32 v13, v4, v5
	v_add_f32_e32 v14, v6, v7
	v_pk_mul_f32 v[26:27], v[76:77], v[18:19] op_sel_hi:[0,1]
	v_pk_mul_f32 v[32:33], v[76:77], v[20:21] op_sel_hi:[0,1]
	v_add_f32_e32 v13, v14, v13
	v_add_f32_e32 v14, v24, v25
	v_add_f32_e32 v15, v2, v3
	v_pk_mul_f32 v[92:93], v[76:77], v[22:23] op_sel_hi:[0,1]
	v_pk_mul_f32 v[94:95], v[76:77], v[28:29] op_sel_hi:[0,1]
	v_add_f32_e32 v14, v15, v14
	v_add_f32_e32 v15, v32, v33
	v_add_f32_e32 v16, v26, v27
	v_pk_mul_f32 v[96:97], v[76:77], v[30:31] op_sel_hi:[0,1]
	v_pk_mul_f32 v[28:29], v[76:77], v[34:35] op_sel_hi:[0,1]
	v_add_f32_e32 v15, v16, v15
	v_add_f32_e32 v16, v94, v95
	v_add_f32_e32 v17, v92, v93
	v_pk_mul_f32 v[30:31], v[76:77], v[36:37] op_sel_hi:[0,1]
	v_pk_mul_f32 v[18:19], v[76:77], v[38:39] op_sel_hi:[0,1]
	v_pk_mul_f32 v[20:21], v[76:77], v[40:41] op_sel_hi:[0,1]
	v_pk_mul_f32 v[22:23], v[76:77], v[42:43] op_sel_hi:[0,1]
	v_pk_mul_f32 v[64:65], v[76:77], v[44:45] op_sel_hi:[0,1]
	v_pk_mul_f32 v[62:63], v[76:77], v[46:47] op_sel_hi:[0,1]
	v_pk_mul_f32 v[60:61], v[76:77], v[48:49] op_sel_hi:[0,1]
	v_pk_mul_f32 v[58:59], v[76:77], v[50:51] op_sel_hi:[0,1]
	v_pk_mul_f32 v[56:57], v[76:77], v[52:53] op_sel_hi:[0,1]
	v_pk_mul_f32 v[40:41], v[76:77], v[54:55] op_sel_hi:[0,1]
	v_pk_mul_f32 v[42:43], v[76:77], v[182:183] op_sel_hi:[0,1]
	v_pk_mul_f32 v[48:49], v[76:77], v[184:185] op_sel_hi:[0,1]
	v_pk_mul_f32 v[50:51], v[76:77], v[186:187] op_sel_hi:[0,1]
	v_pk_mul_f32 v[52:53], v[76:77], v[188:189] op_sel_hi:[0,1]
	v_pk_mul_f32 v[54:55], v[76:77], v[190:191] op_sel_hi:[0,1]
	v_pk_mul_f32 v[44:45], v[76:77], v[192:193] op_sel_hi:[0,1]
	v_pk_mul_f32 v[46:47], v[76:77], v[194:195] op_sel_hi:[0,1]
	v_pk_mul_f32 v[34:35], v[76:77], v[196:197] op_sel_hi:[0,1]
	v_pk_mul_f32 v[36:37], v[76:77], v[198:199] op_sel_hi:[0,1]
	v_pk_mul_f32 v[38:39], v[76:77], v[200:201] op_sel_hi:[0,1]
	v_add_f32_e32 v16, v17, v16
	v_add_f32_e32 v17, v28, v29
	v_add_f32_e32 v76, v96, v97
	v_add_f32_e32 v17, v76, v17
	v_add_f32_e32 v76, v18, v19
	v_add_f32_e32 v87, v30, v31
	v_add_f32_e32 v76, v87, v76
	v_add_f32_e32 v87, v22, v23
	v_add_f32_e32 v89, v20, v21
	v_add_f32_e32 v87, v89, v87
	v_add_f32_e32 v89, v62, v63
	v_add_f32_e32 v91, v64, v65
	v_add_f32_e32 v89, v91, v89
	v_add_f32_e32 v91, v58, v59
	v_add_f32_e32 v182, v60, v61
	v_add_f32_e32 v91, v182, v91
	v_add_f32_e32 v182, v40, v41
	v_add_f32_e32 v183, v56, v57
	v_add_f32_e32 v182, v183, v182
	v_add_f32_e32 v183, v48, v49
	v_add_f32_e32 v184, v42, v43
	v_add_f32_e32 v183, v184, v183
	v_add_f32_e32 v184, v52, v53
	v_add_f32_e32 v185, v50, v51
	v_add_f32_e32 v184, v185, v184
	v_add_f32_e32 v185, v44, v45
	v_add_f32_e32 v186, v54, v55
	v_add_f32_e32 v185, v186, v185
	v_add_f32_e32 v186, v34, v35
	v_add_f32_e32 v187, v46, v47
	v_add_f32_e32 v186, v187, v186
	v_add_f32_e32 v187, v38, v39
	v_add_f32_e32 v188, v36, v37
	v_add_f32_e32 v187, v188, v187
	v_mov_b32_e32 v188, v9
	v_mov_b32_e32 v189, v9
	s_nop 1
	v_permlane32_swap_b32_e32 v188, v189
	v_cndmask_b32_e64 v188, v188, v189, s[2:3]
	v_cndmask_b32_e64 v189, v188, 0, s[4:5]
	v_add_f32_e32 v12, v189, v12
	v_mov_b32_e32 v189, v5
	v_mov_b32_e32 v190, v5
	s_nop 1
	v_permlane32_swap_b32_e32 v189, v190
	v_cndmask_b32_e64 v189, v189, v190, s[2:3]
	v_cndmask_b32_e64 v188, v189, v188, s[4:5]
	v_add_f32_e32 v188, v188, v13
	v_mov_b32_e32 v13, v25
	v_mov_b32_e32 v190, v25
	s_nop 1
	v_permlane32_swap_b32_e32 v13, v190
	v_cndmask_b32_e64 v13, v13, v190, s[2:3]
	v_cndmask_b32_e64 v189, v13, v189, s[4:5]
	v_add_f32_e32 v189, v189, v14
	v_mov_b32_e32 v14, v33
	v_mov_b32_e32 v190, v33
	s_nop 1
	v_permlane32_swap_b32_e32 v14, v190
	v_cndmask_b32_e64 v14, v14, v190, s[2:3]
	v_cndmask_b32_e64 v13, v14, v13, s[4:5]
	v_add_f32_e32 v190, v15, v13
	v_mov_b32_e32 v13, v95
	v_mov_b32_e32 v15, v95
	s_nop 1
	v_permlane32_swap_b32_e32 v13, v15
	v_cndmask_b32_e64 v13, v13, v15, s[2:3]
	v_cndmask_b32_e64 v14, v13, v14, s[4:5]
	v_add_f32_e32 v191, v16, v14
	v_mov_b32_e32 v14, v29
	v_mov_b32_e32 v15, v29
	s_nop 1
	v_permlane32_swap_b32_e32 v14, v15
	v_cndmask_b32_e64 v14, v14, v15, s[2:3]
	v_cndmask_b32_e64 v13, v14, v13, s[4:5]
	v_add_f32_e32 v192, v17, v13
	v_mov_b32_e32 v13, v19
	v_mov_b32_e32 v15, v19
	s_nop 1
	v_permlane32_swap_b32_e32 v13, v15
	v_cndmask_b32_e64 v13, v13, v15, s[2:3]
	v_cndmask_b32_e64 v14, v13, v14, s[4:5]
	v_add_f32_e32 v193, v76, v14
	v_mov_b32_e32 v14, v23
	v_mov_b32_e32 v15, v23
	s_nop 1
	v_permlane32_swap_b32_e32 v14, v15
	v_cndmask_b32_e64 v14, v14, v15, s[2:3]
	v_cndmask_b32_e64 v13, v14, v13, s[4:5]
	v_add_f32_e32 v194, v87, v13
	v_mov_b32_e32 v13, v63
	v_mov_b32_e32 v15, v63
	s_nop 1
	v_permlane32_swap_b32_e32 v13, v15
	v_cndmask_b32_e64 v13, v13, v15, s[2:3]
	v_cndmask_b32_e64 v14, v13, v14, s[4:5]
	v_add_f32_e32 v195, v89, v14
	v_mov_b32_e32 v14, v59
	v_mov_b32_e32 v15, v59
	s_nop 1
	v_permlane32_swap_b32_e32 v14, v15
	v_cndmask_b32_e64 v14, v14, v15, s[2:3]
	v_cndmask_b32_e64 v13, v14, v13, s[4:5]
	v_add_f32_e32 v196, v91, v13
	v_mov_b32_e32 v13, v41
	v_mov_b32_e32 v15, v41
	s_nop 1
	v_permlane32_swap_b32_e32 v13, v15
	v_cndmask_b32_e64 v13, v13, v15, s[2:3]
	v_cndmask_b32_e64 v14, v13, v14, s[4:5]
	v_add_f32_e32 v197, v182, v14
	v_mov_b32_e32 v14, v49
	v_mov_b32_e32 v15, v49
	s_nop 1
	v_permlane32_swap_b32_e32 v14, v15
	v_cndmask_b32_e64 v14, v14, v15, s[2:3]
	v_cndmask_b32_e64 v13, v14, v13, s[4:5]
	v_add_f32_e32 v198, v183, v13
	v_mov_b32_e32 v13, v53
	v_mov_b32_e32 v15, v53
	s_nop 1
	v_permlane32_swap_b32_e32 v13, v15
	v_cndmask_b32_e64 v13, v13, v15, s[2:3]
	v_cndmask_b32_e64 v14, v13, v14, s[4:5]
	v_add_f32_e32 v199, v184, v14
	v_mov_b32_e32 v14, v45
	v_mov_b32_e32 v15, v45
	s_nop 1
	v_permlane32_swap_b32_e32 v14, v15
	v_cndmask_b32_e64 v14, v14, v15, s[2:3]
	v_cndmask_b32_e64 v13, v14, v13, s[4:5]
	v_add_f32_e32 v200, v185, v13
	v_mov_b32_e32 v13, v35
	v_mov_b32_e32 v15, v35
	s_nop 1
	v_permlane32_swap_b32_e32 v13, v15
	v_cndmask_b32_e64 v13, v13, v15, s[2:3]
	v_cndmask_b32_e64 v14, v13, v14, s[4:5]
	v_add_f32_e32 v201, v186, v14
	v_mov_b32_e32 v14, v39
	v_mov_b32_e32 v15, v39
	s_nop 1
	v_permlane32_swap_b32_e32 v14, v15
	v_cndmask_b32_e64 v14, v14, v15, s[2:3]
	v_cndmask_b32_e64 v13, v14, v13, s[4:5]
	v_add_f32_e32 v202, v187, v13
	v_add_f32_dpp v12, v12, v12 quad_perm:[1,0,3,2] row_mask:0xf bank_mask:0xf bound_ctrl:1
	v_mov_b32_e32 v13, v77
	v_add_f32_dpp v14, v188, v188 quad_perm:[1,0,3,2] row_mask:0xf bank_mask:0xf bound_ctrl:1
	v_mov_b32_e32 v15, v77
	v_add_f32_dpp v16, v189, v189 quad_perm:[1,0,3,2] row_mask:0xf bank_mask:0xf bound_ctrl:1
	v_mov_b32_e32 v17, v77
	v_add_f32_dpp v76, v190, v190 quad_perm:[1,0,3,2] row_mask:0xf bank_mask:0xf bound_ctrl:1
	v_mov_b32_e32 v87, v77
	v_add_f32_dpp v89, v191, v191 quad_perm:[1,0,3,2] row_mask:0xf bank_mask:0xf bound_ctrl:1
	v_mov_b32_e32 v91, v77
	v_add_f32_dpp v182, v192, v192 quad_perm:[1,0,3,2] row_mask:0xf bank_mask:0xf bound_ctrl:1
	v_mov_b32_e32 v183, v77
	v_add_f32_dpp v184, v193, v193 quad_perm:[1,0,3,2] row_mask:0xf bank_mask:0xf bound_ctrl:1
	v_mov_b32_e32 v185, v77
	v_add_f32_dpp v186, v194, v194 quad_perm:[1,0,3,2] row_mask:0xf bank_mask:0xf bound_ctrl:1
	v_mov_b32_e32 v187, v77
	v_add_f32_dpp v188, v195, v195 quad_perm:[1,0,3,2] row_mask:0xf bank_mask:0xf bound_ctrl:1
	v_mov_b32_e32 v189, v77
	v_add_f32_dpp v190, v196, v196 quad_perm:[1,0,3,2] row_mask:0xf bank_mask:0xf bound_ctrl:1
	v_mov_b32_e32 v191, v77
	v_add_f32_dpp v192, v197, v197 quad_perm:[1,0,3,2] row_mask:0xf bank_mask:0xf bound_ctrl:1
	v_mov_b32_e32 v193, v77
	v_add_f32_dpp v194, v198, v198 quad_perm:[1,0,3,2] row_mask:0xf bank_mask:0xf bound_ctrl:1
	v_mov_b32_e32 v195, v77
	v_add_f32_dpp v196, v199, v199 quad_perm:[1,0,3,2] row_mask:0xf bank_mask:0xf bound_ctrl:1
	v_mov_b32_e32 v197, v77
	v_add_f32_dpp v198, v200, v200 quad_perm:[1,0,3,2] row_mask:0xf bank_mask:0xf bound_ctrl:1
	v_mov_b32_e32 v199, v77
	v_add_f32_dpp v200, v201, v201 quad_perm:[1,0,3,2] row_mask:0xf bank_mask:0xf bound_ctrl:1
	v_mov_b32_e32 v201, v77
	v_add_f32_dpp v202, v202, v202 quad_perm:[1,0,3,2] row_mask:0xf bank_mask:0xf bound_ctrl:1
	v_mov_b32_dpp v13, v12 quad_perm:[2,3,0,1] row_mask:0xf bank_mask:0xf
	v_mov_b32_dpp v15, v14 quad_perm:[2,3,0,1] row_mask:0xf bank_mask:0xf
	v_mov_b32_dpp v17, v16 quad_perm:[2,3,0,1] row_mask:0xf bank_mask:0xf
	v_mov_b32_dpp v87, v76 quad_perm:[2,3,0,1] row_mask:0xf bank_mask:0xf
	v_mov_b32_dpp v91, v89 quad_perm:[2,3,0,1] row_mask:0xf bank_mask:0xf
	v_mov_b32_dpp v183, v182 quad_perm:[2,3,0,1] row_mask:0xf bank_mask:0xf
	v_mov_b32_dpp v185, v184 quad_perm:[2,3,0,1] row_mask:0xf bank_mask:0xf
	v_mov_b32_dpp v187, v186 quad_perm:[2,3,0,1] row_mask:0xf bank_mask:0xf
	v_mov_b32_dpp v189, v188 quad_perm:[2,3,0,1] row_mask:0xf bank_mask:0xf
	v_mov_b32_dpp v191, v190 quad_perm:[2,3,0,1] row_mask:0xf bank_mask:0xf
	v_mov_b32_dpp v193, v192 quad_perm:[2,3,0,1] row_mask:0xf bank_mask:0xf
	v_mov_b32_dpp v195, v194 quad_perm:[2,3,0,1] row_mask:0xf bank_mask:0xf
	v_mov_b32_dpp v197, v196 quad_perm:[2,3,0,1] row_mask:0xf bank_mask:0xf
	v_mov_b32_dpp v199, v198 quad_perm:[2,3,0,1] row_mask:0xf bank_mask:0xf
	v_mov_b32_dpp v201, v200 quad_perm:[2,3,0,1] row_mask:0xf bank_mask:0xf
	v_mov_b32_dpp v203, v202 quad_perm:[2,3,0,1] row_mask:0xf bank_mask:0xf
	s_and_saveexec_b64 s[10:11], s[6:7]
	s_cbranch_execz .LBB0_556
	v_add_f32_e32 v12, v12, v13
	v_lshlrev_b32_e32 v13, 2, v74
	v_add_f32_e32 v14, v14, v15
	v_add3_u32 v13, s40, v158, v13
	v_add_f32_e32 v202, v202, v203
	v_add_f32_e32 v200, v200, v201
	v_add_f32_e32 v198, v198, v199
	v_add_f32_e32 v196, v196, v197
	v_add_f32_e32 v194, v194, v195
	v_add_f32_e32 v192, v192, v193
	v_add_f32_e32 v190, v190, v191
	v_add_f32_e32 v188, v188, v189
	v_add_f32_e32 v186, v186, v187
	v_add_f32_e32 v184, v184, v185
	v_add_f32_e32 v182, v182, v183
	v_add_f32_e32 v89, v89, v91
	v_add_f32_e32 v76, v76, v87
	v_add_f32_e32 v16, v16, v17
	ds_write2_b32 v13, v12, v14 offset1:2
	ds_write2_b32 v13, v16, v76 offset0:4 offset1:6
	ds_write2_b32 v13, v89, v182 offset0:8 offset1:10
	ds_write2_b32 v13, v184, v186 offset0:12 offset1:14
	ds_write2_b32 v13, v188, v190 offset0:16 offset1:18
	ds_write2_b32 v13, v192, v194 offset0:20 offset1:22
	ds_write2_b32 v13, v196, v198 offset0:24 offset1:26
	ds_write2_b32 v13, v200, v202 offset0:28 offset1:30

.LBB0_641:
	s_or_b64 exec, exec, s[2:3]
	s_mov_b32 s100, 4
	s_waitcnt lgkmcnt(0)
	s_barrier
	ds_read_b32 v2, v172
	s_mov_b64 s[2:3], -1
	s_waitcnt lgkmcnt(0)
	v_cmp_le_i32_e32 vcc, s15, v2
	v_readfirstlane_b32 s6, v2
	s_cbranch_vccnz .LBB0_636
	s_add_i32 s2, s6, 0xfffffe00
	s_cmpk_gt_i32 s6, 0x1ff
	s_cselect_b32 s2, s2, s6
	s_ashr_i32 s3, s2, 31
	s_lshr_b32 s3, s3, 26
	s_add_i32 s3, s2, s3
	s_ashr_i32 s10, s3, 6
	s_andn2_b32 s3, s3, 63
	v_mov_b32_e32 v14, v0
	s_sub_i32 s11, s2, s3
	s_and_b32 s2, s11, 3
	v_readfirstlane_b32 s43, v14
	s_ashr_i32 s41, s43, 6
	s_sub_i32 s44, 7, s10
	s_ashr_i32 s45, s43, 8
	s_and_b32 s12, s41, 3
	s_lshl_b32 s2, s2, 1
	s_ashr_i32 s8, s11, 2
	s_add_i32 s33, s45, s2
	s_lshl_b32 s2, s44, 8
	s_lshl_b32 s54, s12, 6
	s_ashr_i32 s9, s8, 31
	s_or_b32 s42, s54, s2
	s_lshl_b32 s2, s33, 6
	s_ashr_i32 s3, s2, 31
	s_lshl_b64 s[6:7], s[8:9], 21
	v_and_b32_e32 v177, 31, v14
	s_add_u32 s13, s16, s6
	v_or_b32_e32 v162, s42, v177
	s_addc_u32 s46, s17, s7
	s_lshl_b64 s[6:7], s[2:3], 1
	v_or_b32_e32 v164, 32, v162
	s_add_u32 s2, s13, s6
	v_mov_b32_e32 v165, v163
	s_addc_u32 s3, s46, s7
	v_lshlrev_b64 v[2:3], 10, v[162:163]
	v_lshlrev_b64 v[6:7], 10, v[164:165]
	v_lshl_add_u64 v[2:3], s[2:3], 0, v[2:3]
	v_lshl_add_u64 v[6:7], s[2:3], 0, v[6:7]
	s_lshl_b32 s2, s8, 1
	s_bfe_u32 s11, s11, 0x10001
	s_or_b32 s2, s11, s2
	s_ashr_i32 s3, s2, 31
	v_bfe_u32 v176, v14, 5, 1
	s_lshl_b64 s[2:3], s[2:3], 13
	v_lshlrev_b32_e32 v4, 4, v176
	v_mov_b32_e32 v5, v163
	s_add_u32 s2, s18, s2
	v_lshl_add_u64 v[6:7], v[6:7], 0, v[4:5]
	s_addc_u32 s3, s19, s3
	v_lshl_add_u64 v[2:3], v[2:3], 0, v[4:5]
	v_lshl_add_u64 v[8:9], v[162:163], 2, s[2:3]
	global_load_dwordx4 v[130:133], v[6:7], off offset:96
	global_load_dwordx4 v[138:141], v[6:7], off offset:64
	global_load_dwordx4 v[134:137], v[2:3], off offset:96
	global_load_dwordx4 v[142:145], v[2:3], off offset:64
	global_load_dwordx4 v[146:149], v[6:7], off offset:32
	global_load_dwordx4 v[154:157], v[6:7], off
	global_load_dwordx4 v[150:153], v[2:3], off offset:32
	global_load_dwordx4 v[158:161], v[2:3], off
	global_load_dword v184, v[8:9], off
	global_load_dword v183, v[8:9], off offset:128
	v_lshlrev_b32_e32 v6, 6, v14
	v_and_b32_e32 v6, 0xf00, v6
	v_lshl_or_b32 v6, s12, 12, v6
	s_lshl_b64 s[12:13], s[8:9], 19
	s_lshl_b32 s11, s11, 7
	s_or_b32 s55, s12, s11
	s_add_u32 s2, s20, s55
	v_and_b32_e32 v180, 63, v14
	s_addc_u32 s3, s21, s13
	v_mov_b32_e32 v3, v163
	v_lshlrev_b32_e32 v2, 8, v180
	s_add_u32 s46, s22, s55
	v_lshl_add_u64 v[10:11], s[2:3], 0, v[2:3]
	s_addc_u32 s47, s23, s13
	s_lshl_b32 s2, s41, 3
	s_lshl_b32 s48, s45, 5
	v_mov_b32_e32 v7, v163
	v_lshlrev_b32_e32 v178, 3, v14
	s_lshl_b32 s45, s41, 10
	s_ashr_i32 s3, s2, 31
	s_ashr_i32 s49, s48, 31
	v_and_b32_e32 v16, 24, v178
	v_lshl_add_u64 v[12:13], s[46:47], 0, v[6:7]
	s_add_i32 s45, s45, 0
	s_lshl_b64 s[50:51], s[2:3], 1
	s_lshl_b64 s[52:53], s[48:49], 1
	v_mov_b32_e32 v15, v163
	v_mov_b32_e32 v9, v163
	v_lshlrev_b32_e32 v8, 1, v16
	s_add_i32 s2, s45, 0x8000
	v_lshl_add_u64 v[10:11], v[10:11], 0, s[50:51]
	v_lshl_add_u64 v[12:13], v[12:13], 0, s[52:53]
	s_mov_b32 m0, s45
	v_lshl_add_u64 v[8:9], v[12:13], 0, v[8:9]
	v_lshlrev_b32_e32 v179, 2, v176
	s_lshl_b32 s49, s10, 2
	s_lshl_b32 s10, s10, 8
	s_sub_i32 s10, s54, s10
	s_or_b32 s48, s42, 63
	s_sub_i32 s49, 31, s49
	s_addk_i32 s10, 0x700
	v_mov_b32_e32 v34, v163
	v_mov_b32_e32 v35, v163
	v_mov_b32_e32 v48, v163
	v_mov_b32_e32 v49, v163
	v_mov_b32_e32 v36, v163
	v_mov_b32_e32 v37, v163
	v_mov_b32_e32 v38, v163
	v_mov_b32_e32 v39, v163
	s_barrier
	global_load_lds_dwordx4 v[10:11], off
	s_mov_b32 m0, s2
	s_and_b32 s2, s43, 0x3fffffc0
	global_load_lds_dwordx4 v[8:9], off
	s_lshl_b32 s2, s2, 2
	s_add_i32 s2, s2, 0
	v_lshlrev_b32_e32 v5, 1, v14
	v_lshrrev_b32_e32 v8, 2, v14
	s_add_i32 s43, s2, 0x10400
	v_and_b32_e32 v5, 32, v5
	v_and_or_b32 v8, v8, 3, v179
	v_lshlrev_b32_e32 v8, 6, v8
	v_lshl_add_u32 v174, v177, 2, s43
	v_add_u32_e32 v165, s43, v4
	s_or_b32 s43, s42, 32
	v_add_u32_e32 v4, 0, v5
	v_add3_u32 v182, v4, v8, v16
	v_or_b32_e32 v4, s10, v177
	s_add_u32 s10, s34, s50
	s_addc_u32 s50, s35, s51
	s_add_u32 s10, s10, s11
	s_addc_u32 s11, s50, 0
	s_add_u32 s10, s10, s12
	s_addc_u32 s11, s11, s13
	v_lshl_add_u64 v[166:167], s[10:11], 0, v[2:3]
	s_add_u32 s10, s52, s55
	v_and_b32_e32 v2, 3, v14
	s_addc_u32 s11, s53, s13
	v_lshl_or_b32 v2, v2, 4, s10
	v_mov_b32_e32 v3, s11
	s_waitcnt vmcnt(0)
	v_lshlrev_b32_e32 v9, 10, v176
	v_lshlrev_b32_e32 v10, 4, v177
	v_lshl_add_u64 v[2:3], v[2:3], 0, v[6:7]
	v_add3_u32 v185, 0, v9, v10
	v_sub_u32_e32 v188, v4, v179
	v_lshl_add_u64 v[168:169], s[4:5], 0, v[2:3]
	v_mov_b32_e32 v40, v163
	v_mov_b32_e32 v41, v163
	v_mov_b32_e32 v42, v163
	v_mov_b32_e32 v43, v163
	v_mov_b32_e32 v44, v163
	v_mov_b32_e32 v45, v163
	v_mov_b32_e32 v46, v163
	v_mov_b32_e32 v47, v163
	v_mov_b64_e32 v[64:65], v[48:49]
	v_mov_b64_e32 v[2:3], v[34:35]
	v_mov_b64_e32 v[18:19], v[34:35]
	s_mov_b32 s46, 63
	s_mov_b32 s47, 0
	v_or_b32_e32 v186, v184, v183
	v_cmp_gt_u32_e64 s[2:3], 32, v180
	v_mov_b32_e32 v189, 0
	s_mov_b64 s[10:11], 0
	v_mov_b64_e32 v[62:63], v[46:47]
	v_mov_b64_e32 v[60:61], v[44:45]
	v_mov_b64_e32 v[58:59], v[42:43]
	v_mov_b64_e32 v[56:57], v[40:41]
	v_mov_b64_e32 v[54:55], v[38:39]
	v_mov_b64_e32 v[52:53], v[36:37]
	v_mov_b64_e32 v[50:51], v[34:35]
	v_mov_b64_e32 v[4:5], v[36:37]
	v_mov_b64_e32 v[6:7], v[38:39]
	v_mov_b64_e32 v[8:9], v[40:41]
	v_mov_b64_e32 v[10:11], v[42:43]
	v_mov_b64_e32 v[12:13], v[44:45]
	v_mov_b64_e32 v[14:15], v[46:47]
	v_mov_b64_e32 v[16:17], v[48:49]
	v_mov_b64_e32 v[20:21], v[36:37]
	v_mov_b64_e32 v[22:23], v[38:39]
	v_mov_b64_e32 v[24:25], v[40:41]
	v_mov_b64_e32 v[26:27], v[42:43]
	v_mov_b64_e32 v[28:29], v[44:45]
	v_mov_b64_e32 v[30:31], v[46:47]
	v_mov_b64_e32 v[32:33], v[48:49]
	v_mov_b32_e32 v181, 0
	v_mov_b32_e32 v187, 0
	v_mov_b32_e32 v175, 0
	s_waitcnt vmcnt(0) lgkmcnt(0)
	s_barrier
	s_branch .LBB0_646
